# speedup vs baseline: 1.0055x; 1.0055x over previous
.LBB1_8:
	s_or_b64 exec, exec, s[4:5]
	s_waitcnt vmcnt(0) lgkmcnt(0)
	v_lshl_or_b32 v186, s19, 6, v1
	v_ashrrev_i32_e32 v187, 31, v186
	v_lshl_add_u64 v[186:187], v[186:187], 2, s[6:7]
	global_load_dword v175, v[186:187], off
	v_mov_b32_e32 v184, 1
	v_lshl_add_u32 v180, v176, 2, v172
	v_lshl_add_u32 v181, v177, 2, v172
	v_lshl_add_u32 v182, v178, 2, v172
	v_lshl_add_u32 v183, v179, 2, v172
	s_waitcnt lgkmcnt(0)
	ds_add_u32 v180, v184
	ds_add_u32 v181, v184
	ds_add_u32 v182, v184
	ds_add_u32 v183, v184
	s_waitcnt lgkmcnt(0)
	ds_read_b32 v151, v173
	s_waitcnt lgkmcnt(0)
	v_cvt_f32_i32_e32 v185, v151
	ds_write_b32 v173, v185 offset:256
	v_add_u32_e32 v10, v172, v2
	s_waitcnt vmcnt(1) lgkmcnt(0)
	s_barrier
	ds_read_b128 v[18:21], v10 offset:256
	ds_read_b128 v[22:25], v10 offset:288
	ds_read_b128 v[82:85], v10 offset:320
	ds_read_b128 v[86:89], v10 offset:352
	ds_read_b128 v[74:77], v10 offset:384
	ds_read_b128 v[78:81], v10 offset:416
	ds_read_b128 v[2:5], v213 offset:32768
	ds_read_b128 v[6:9], v213 offset:0
	ds_read_b128 v[66:69], v10 offset:448
	ds_read_b128 v[70:73], v10 offset:480
	ds_read_b128 v[10:13], v213 offset:1024
	s_waitcnt lgkmcnt(3)
	v_pk_mul_f32 v[26:27], v[8:9], v[20:21]
	v_pk_mul_f32 v[28:29], v[6:7], v[18:19]
	ds_read_b128 v[14:17], v213 offset:8192
	s_waitcnt lgkmcnt(1)
	v_pk_mul_f32 v[12:13], v[12:13], v[24:25]
	v_pk_mul_f32 v[10:11], v[10:11], v[22:23]
	v_pk_fma_f32 v[30:31], v[8:9], v[20:21], v[12:13]
	v_pk_fma_f32 v[32:33], v[6:7], v[18:19], v[10:11]
	v_cvt_pk_bf16_f32 v9, v12, v13
	v_cvt_pk_bf16_f32 v7, v26, v27
	v_cvt_pk_bf16_f32 v8, v10, v11
	v_cvt_pk_bf16_f32 v6, v28, v29
	ds_read_b128 v[10:13], v213 offset:33792
	s_nop 0
	v_mfma_f32_32x32x16_bf16 v[34:49], v[2:5], v[6:9], 0
	ds_read_b128 v[6:9], v213 offset:9216
	s_waitcnt lgkmcnt(2)
	v_mul_f32_e32 v26, v16, v20
	v_mul_f32_e32 v27, v17, v21
	v_pk_mul_f32 v[50:51], v[14:15], v[18:19]
	s_mov_b32 s4, 0x3727c5ac
	s_waitcnt lgkmcnt(0)
	v_pk_mul_f32 v[8:9], v[8:9], v[24:25]
	v_pk_mul_f32 v[28:29], v[6:7], v[22:23]
	v_pk_fma_f32 v[90:91], v[16:17], v[20:21], v[8:9]
	v_pk_fma_f32 v[92:93], v[14:15], v[18:19], v[28:29]
	ds_read_b128 v[14:17], v213 offset:2048
	v_cvt_pk_bf16_f32 v9, v8, v9
	v_cvt_pk_bf16_f32 v7, v26, v27
	v_cvt_pk_bf16_f32 v8, v28, v29
	ds_read_b128 v[26:29], v213 offset:3072
	v_cvt_pk_bf16_f32 v6, v50, v51
	s_waitcnt lgkmcnt(1)
	v_pk_mul_f32 v[94:95], v[14:15], v[82:83]
	s_mov_b32 s0, 0x3c800000
	v_mfma_f32_32x32x16_bf16 v[50:65], v[2:5], v[6:9], 0
	v_mul_f32_e32 v2, v16, v84
	v_mul_f32_e32 v3, v17, v85
	s_waitcnt lgkmcnt(0)
	v_mul_f32_e32 v4, v28, v88
	v_mul_f32_e32 v5, v29, v89
	v_pk_mul_f32 v[6:7], v[26:27], v[86:87]
	v_pk_fma_f32 v[8:9], v[16:17], v[84:85], v[4:5]
	v_cvt_pk_bf16_f32 v3, v2, v3
	v_pk_fma_f32 v[14:15], v[14:15], v[82:83], v[6:7]
	v_pk_add_f32 v[26:27], v[8:9], v[30:31]
	v_cvt_pk_bf16_f32 v5, v4, v5
	v_cvt_pk_bf16_f32 v4, v6, v7
	ds_read_b128 v[6:9], v213 offset:10240
	v_pk_add_f32 v[28:29], v[14:15], v[32:33]
	ds_read_b128 v[14:17], v213 offset:11264
	v_cvt_pk_bf16_f32 v2, v94, v95
	s_waitcnt lgkmcnt(1)
	v_pk_mul_f32 v[30:31], v[6:7], v[82:83]
	v_mov_b64_e32 v[152:153], s[4:5]
	v_mfma_f32_32x32x16_bf16 v[34:49], v[10:13], v[2:5], v[34:49]
	v_mul_f32_e32 v2, v8, v84
	v_mul_f32_e32 v3, v9, v85
	s_waitcnt lgkmcnt(0)
	v_mul_f32_e32 v4, v16, v88
	v_mul_f32_e32 v5, v17, v89
	v_pk_mul_f32 v[14:15], v[14:15], v[86:87]
	v_pk_fma_f32 v[8:9], v[8:9], v[84:85], v[4:5]
	v_pk_fma_f32 v[6:7], v[6:7], v[82:83], v[14:15]
	v_cvt_pk_bf16_f32 v5, v4, v5
	v_cvt_pk_bf16_f32 v3, v2, v3
	v_cvt_pk_bf16_f32 v4, v14, v15
	v_pk_add_f32 v[32:33], v[8:9], v[90:91]
	v_pk_add_f32 v[90:91], v[6:7], v[92:93]
	ds_read_b128 v[6:9], v213 offset:34816
	ds_read_b128 v[14:17], v213 offset:4096
	v_cvt_pk_bf16_f32 v2, v30, v31
	s_mov_b32 s13, 0
	s_mov_b64 s[6:7], 0
	v_mfma_f32_32x32x16_bf16 v[50:65], v[10:13], v[2:5], v[50:65]
	ds_read_b128 v[2:5], v213 offset:5120
	ds_read_b128 v[10:13], v213 offset:12288
	s_waitcnt lgkmcnt(2)
	v_pk_mul_f32 v[30:31], v[16:17], v[76:77]
	v_pk_mul_f32 v[92:93], v[14:15], v[74:75]
	s_waitcnt lgkmcnt(1)
	v_pk_mul_f32 v[4:5], v[4:5], v[80:81]
	v_pk_mul_f32 v[94:95], v[2:3], v[78:79]
	v_pk_fma_f32 v[2:3], v[16:17], v[76:77], v[4:5]
	v_cvt_pk_bf16_f32 v5, v4, v5
	v_pk_add_f32 v[96:97], v[2:3], v[26:27]
	v_cvt_pk_bf16_f32 v3, v30, v31
	v_cvt_pk_bf16_f32 v4, v94, v95
	v_cvt_pk_bf16_f32 v2, v92, v93
	v_pk_fma_f32 v[14:15], v[14:15], v[74:75], v[94:95]
	s_waitcnt lgkmcnt(0)
	v_pk_mul_f32 v[30:31], v[10:11], v[74:75]
	v_mfma_f32_32x32x16_bf16 v[34:49], v[6:9], v[2:5], v[34:49]
	ds_read_b128 v[2:5], v213 offset:13312
	v_add_f32_e32 v98, v14, v28
	v_add_f32_e32 v99, v15, v29
	ds_read_b128 v[14:17], v213 offset:35840
	v_pk_mul_f32 v[26:27], v[12:13], v[76:77]
	s_waitcnt lgkmcnt(1)
	v_pk_mul_f32 v[4:5], v[4:5], v[80:81]
	v_pk_mul_f32 v[28:29], v[2:3], v[78:79]
	v_pk_fma_f32 v[2:3], v[12:13], v[76:77], v[4:5]
	v_pk_fma_f32 v[10:11], v[10:11], v[74:75], v[28:29]
	v_pk_add_f32 v[32:33], v[2:3], v[32:33]
	v_pk_add_f32 v[92:93], v[10:11], v[90:91]
	ds_read_b128 v[10:13], v213 offset:6144
	v_cvt_pk_bf16_f32 v5, v4, v5
	v_cvt_pk_bf16_f32 v3, v26, v27
	v_cvt_pk_bf16_f32 v4, v28, v29
	ds_read_b128 v[26:29], v213 offset:7168
	v_cvt_pk_bf16_f32 v2, v30, v31
	s_waitcnt lgkmcnt(1)
	v_pk_mul_f32 v[30:31], v[10:11], v[66:67]
	v_mfma_f32_32x32x16_bf16 v[50:65], v[6:9], v[2:5], v[50:65]
	v_mul_f32_e32 v2, v12, v68
	v_mul_f32_e32 v3, v13, v69
	s_waitcnt lgkmcnt(0)
	v_mul_f32_e32 v4, v28, v72
	v_mul_f32_e32 v5, v29, v73
	v_pk_mul_f32 v[6:7], v[26:27], v[70:71]
	v_pk_fma_f32 v[8:9], v[12:13], v[68:69], v[4:5]
	v_cvt_pk_bf16_f32 v3, v2, v3
	v_pk_fma_f32 v[10:11], v[10:11], v[66:67], v[6:7]
	v_pk_add_f32 v[94:95], v[8:9], v[96:97]
	v_cvt_pk_bf16_f32 v5, v4, v5
	v_cvt_pk_bf16_f32 v4, v6, v7
	ds_read_b128 v[6:9], v213 offset:14336
	v_pk_add_f32 v[96:97], v[10:11], v[98:99]
	ds_read_b128 v[10:13], v213 offset:15360
	v_cvt_pk_bf16_f32 v2, v30, v31
	s_waitcnt lgkmcnt(1)
	v_pk_mul_f32 v[30:31], v[6:7], v[66:67]
	v_mfma_f32_32x32x16_bf16 v[34:49], v[14:17], v[2:5], v[34:49]
	s_waitcnt lgkmcnt(0)
	v_mul_f32_e32 v10, v10, v70
	v_mul_f32_e32 v11, v11, v71
	v_mul_f32_e32 v2, v8, v68
	v_mul_f32_e32 v3, v9, v69
	v_pk_mul_f32 v[4:5], v[12:13], v[72:73]
	v_pk_fma_f32 v[6:7], v[6:7], v[66:67], v[10:11]
	v_pk_fma_f32 v[8:9], v[8:9], v[68:69], v[4:5]
	v_pk_add_f32 v[92:93], v[6:7], v[92:93]
	v_cvt_pk_bf16_f32 v3, v2, v3
	v_pk_add_f32 v[90:91], v[8:9], v[32:33]
	v_cvt_pk_bf16_f32 v5, v4, v5
	v_cvt_pk_bf16_f32 v4, v10, v11
	ds_read_b128 v[26:29], v213 offset:36864
	ds_read_b128 v[6:9], v213 offset:16384
	v_cvt_pk_bf16_f32 v2, v30, v31
	ds_read_b128 v[98:101], v213 offset:25600
	ds_read_b128 v[102:105], v213 offset:37888
	v_mfma_f32_32x32x16_bf16 v[50:65], v[14:17], v[2:5], v[50:65]
	ds_read_b128 v[2:5], v213 offset:17408
	ds_read_b128 v[30:33], v213 offset:24576
	s_waitcnt lgkmcnt(4)
	v_pk_mul_f32 v[12:13], v[6:7], v[18:19]
	v_pk_mul_f32 v[10:11], v[8:9], v[20:21]
	s_waitcnt lgkmcnt(1)
	v_pk_mul_f32 v[14:15], v[2:3], v[22:23]
	v_pk_mul_f32 v[22:23], v[98:99], v[22:23]
	v_pk_fma_f32 v[112:113], v[6:7], v[18:19], v[14:15]
	s_waitcnt lgkmcnt(0)
	v_pk_mul_f32 v[114:115], v[30:31], v[18:19]
	v_pk_fma_f32 v[118:119], v[30:31], v[18:19], v[22:23]
	v_pk_mul_f32 v[4:5], v[4:5], v[24:25]
	v_pk_mul_f32 v[106:107], v[32:33], v[20:21]
	v_pk_mul_f32 v[24:25], v[100:101], v[24:25]
	ds_read_b128 v[98:101], v213 offset:18432
	v_cvt_pk_bf16_f32 v19, v106, v107
	ds_read_b128 v[106:109], v213 offset:19456
	v_pk_fma_f32 v[110:111], v[8:9], v[20:21], v[4:5]
	v_cvt_pk_bf16_f32 v5, v4, v5
	v_cvt_pk_bf16_f32 v3, v10, v11
	v_cvt_pk_bf16_f32 v4, v14, v15
	s_waitcnt lgkmcnt(0)
	v_pk_mul_f32 v[106:107], v[106:107], v[86:87]
	v_cvt_pk_bf16_f32 v2, v12, v13
	v_pk_mul_f32 v[120:121], v[98:99], v[82:83]
	v_pk_mul_f32 v[108:109], v[108:109], v[88:89]
	v_pk_fma_f32 v[98:99], v[98:99], v[82:83], v[106:107]
	v_mfma_f32_32x32x16_bf16 v[2:17], v[26:29], v[2:5], 0
	v_cvt_pk_bf16_f32 v18, v114, v115
	v_mul_f32_e32 v114, v100, v84
	v_mul_f32_e32 v115, v101, v85
	v_fma_f32 v100, v100, v84, v108
	v_fma_f32 v101, v101, v85, v109
	v_pk_add_f32 v[124:125], v[98:99], v[112:113]
	v_pk_add_f32 v[122:123], v[100:101], v[110:111]
	v_cvt_pk_bf16_f32 v101, v108, v109
	v_cvt_pk_bf16_f32 v100, v106, v107
	ds_read_b128 v[106:109], v213 offset:26624
	v_pk_fma_f32 v[116:117], v[32:33], v[20:21], v[24:25]
	v_cvt_pk_bf16_f32 v21, v24, v25
	v_cvt_pk_bf16_f32 v20, v22, v23
	ds_read_b128 v[110:113], v213 offset:27648
	v_cvt_pk_bf16_f32 v99, v114, v115
	v_mfma_f32_32x32x16_bf16 v[18:33], v[26:29], v[18:21], 0
	v_cvt_pk_bf16_f32 v98, v120, v121
	s_waitcnt lgkmcnt(1)
	v_mul_f32_e32 v114, v106, v82
	v_mul_f32_e32 v115, v107, v83
	s_waitcnt lgkmcnt(0)
	v_pk_mul_f32 v[86:87], v[110:111], v[86:87]
	v_pk_mul_f32 v[88:89], v[112:113], v[88:89]
	v_pk_fma_f32 v[82:83], v[106:107], v[82:83], v[86:87]
	v_mfma_f32_32x32x16_bf16 v[2:17], v[102:105], v[98:101], v[2:17]
	v_mul_f32_e32 v98, v108, v84
	v_mul_f32_e32 v99, v109, v85
	v_fma_f32 v84, v108, v84, v88
	v_fma_f32 v85, v109, v85, v89
	v_add_f32_e32 v108, v82, v118
	v_add_f32_e32 v109, v83, v119
	v_cvt_pk_bf16_f32 v83, v98, v99
	v_pk_add_f32 v[106:107], v[84:85], v[116:117]
	v_cvt_pk_bf16_f32 v85, v88, v89
	v_cvt_pk_bf16_f32 v84, v86, v87
	ds_read_b128 v[86:89], v213 offset:38912
	ds_read_b128 v[98:101], v213 offset:20480
	v_cvt_pk_bf16_f32 v82, v114, v115
	s_waitcnt lgkmcnt(0)
	v_pk_mul_f32 v[110:111], v[100:101], v[76:77]
	v_mfma_f32_32x32x16_bf16 v[18:33], v[102:105], v[82:85], v[18:33]
	ds_read_b128 v[82:85], v213 offset:21504
	ds_read_b128 v[102:105], v213 offset:28672
	v_mul_f32_e32 v112, v98, v74
	v_mul_f32_e32 v113, v99, v75
	s_waitcnt lgkmcnt(1)
	v_pk_mul_f32 v[84:85], v[84:85], v[80:81]
	v_pk_mul_f32 v[114:115], v[82:83], v[78:79]
	v_pk_fma_f32 v[82:83], v[100:101], v[76:77], v[84:85]
	v_cvt_pk_bf16_f32 v85, v84, v85
	v_pk_add_f32 v[116:117], v[82:83], v[122:123]
	v_cvt_pk_bf16_f32 v83, v110, v111
	v_cvt_pk_bf16_f32 v84, v114, v115
	v_cvt_pk_bf16_f32 v82, v112, v113
	v_pk_fma_f32 v[98:99], v[98:99], v[74:75], v[114:115]
	s_waitcnt lgkmcnt(0)
	v_pk_mul_f32 v[112:113], v[102:103], v[74:75]
	v_mfma_f32_32x32x16_bf16 v[2:17], v[86:89], v[82:85], v[2:17]
	ds_read_b128 v[82:85], v213 offset:29696
	v_add_f32_e32 v118, v98, v124
	v_add_f32_e32 v119, v99, v125
	v_mul_f32_e32 v110, v104, v76
	v_mul_f32_e32 v111, v105, v77
	ds_read_b128 v[98:101], v213 offset:39936
	s_waitcnt lgkmcnt(1)
	v_pk_mul_f32 v[78:79], v[82:83], v[78:79]
	v_pk_mul_f32 v[80:81], v[84:85], v[80:81]
	v_pk_fma_f32 v[74:75], v[102:103], v[74:75], v[78:79]
	v_pk_fma_f32 v[76:77], v[104:105], v[76:77], v[80:81]
	v_pk_add_f32 v[104:105], v[74:75], v[108:109]
	v_pk_add_f32 v[102:103], v[76:77], v[106:107]
	v_cvt_pk_bf16_f32 v77, v80, v81
	v_cvt_pk_bf16_f32 v76, v78, v79
	ds_read_b128 v[78:81], v213 offset:22528
	ds_read_b128 v[82:85], v213 offset:23552
	v_cvt_pk_bf16_f32 v75, v110, v111
	v_cvt_pk_bf16_f32 v74, v112, v113
	s_waitcnt lgkmcnt(0)
	v_pk_mul_f32 v[82:83], v[82:83], v[70:71]
	v_mfma_f32_32x32x16_bf16 v[18:33], v[86:89], v[74:77], v[18:33]
	v_mul_f32_e32 v74, v80, v68
	v_mul_f32_e32 v75, v81, v69
	v_mul_f32_e32 v76, v84, v72
	v_mul_f32_e32 v77, v85, v73
	v_mul_f32_e32 v86, v78, v66
	v_mul_f32_e32 v87, v79, v67
	v_pk_fma_f32 v[80:81], v[80:81], v[68:69], v[76:77]
	v_pk_fma_f32 v[78:79], v[78:79], v[66:67], v[82:83]
	v_cvt_pk_bf16_f32 v75, v74, v75
	v_pk_add_f32 v[88:89], v[80:81], v[116:117]
	v_pk_add_f32 v[106:107], v[78:79], v[118:119]
	ds_read_b128 v[78:81], v213 offset:30720
	v_cvt_pk_bf16_f32 v77, v76, v77
	v_cvt_pk_bf16_f32 v76, v82, v83
	ds_read_b128 v[82:85], v213 offset:31744
	v_cvt_pk_bf16_f32 v74, v86, v87
	s_waitcnt lgkmcnt(0)
	v_pk_mul_f32 v[72:73], v[84:85], v[72:73]
	v_mfma_f32_32x32x16_bf16 v[2:17], v[98:101], v[74:77], v[2:17]
	v_mul_f32_e32 v74, v80, v68
	v_mul_f32_e32 v75, v81, v69
	v_fma_f32 v68, v80, v68, v72
	v_fma_f32 v69, v81, v69, v73
	v_mul_f32_e32 v70, v82, v70
	v_mul_f32_e32 v71, v83, v71
	v_pk_add_f32 v[84:85], v[68:69], v[102:103]
	v_cvt_pk_bf16_f32 v69, v72, v73
	v_pk_mov_b32 v[72:73], v[96:97], v[94:95] op_sel:[1,0]
	v_mov_b32_e32 v97, v95
	v_pk_add_f32 v[72:73], v[72:73], v[96:97]
	v_pk_mul_f32 v[76:77], v[78:79], v[66:67]
	v_pk_fma_f32 v[66:67], v[78:79], v[66:67], v[70:71]
	v_pk_add_f32 v[72:73], v[72:73], v[72:73] op_sel:[0,1] op_sel_hi:[1,0]
	v_pk_add_f32 v[86:87], v[66:67], v[104:105]
	v_mov_b32_e32 v66, v72
	s_nop 1
	v_permlane32_swap_b32_e32 v72, v66
	v_add_f32_e32 v66, v72, v66
	v_cvt_pk_bf16_f32 v67, v74, v75
	v_rcp_f32_e32 v74, v66
	v_cvt_pk_bf16_f32 v68, v70, v71
	v_cvt_pk_bf16_f32 v66, v76, v77
	v_pk_mul_f32 v[70:71], v[46:47], v[74:75] op_sel_hi:[1,0]
	s_nop 0
	v_mfma_f32_32x32x16_bf16 v[18:33], v[98:101], v[66:69], v[18:33]
	v_mul_f32_e32 v66, v42, v74
	v_mul_f32_e32 v67, v43, v74
	v_pk_mov_b32 v[42:43], v[92:93], v[90:91] op_sel:[1,0]
	v_mov_b32_e32 v93, v91
	v_pk_add_f32 v[42:43], v[42:43], v[92:93]
	v_pk_mul_f32 v[68:69], v[44:45], v[74:75] op_sel_hi:[1,0]
	v_pk_add_f32 v[42:43], v[42:43], v[42:43] op_sel:[0,1] op_sel_hi:[1,0]
	v_pk_mov_b32 v[44:45], v[106:107], v[88:89] op_sel:[1,0]
	v_mov_b32_e32 v43, v42
	s_nop 1
	v_permlane32_swap_b32_e32 v42, v43
	v_add_f32_e32 v42, v42, v43
	v_rcp_f32_e32 v42, v42
	v_mov_b32_e32 v107, v89
	v_pk_add_f32 v[44:45], v[44:45], v[106:107]
	v_pk_mul_f32 v[72:73], v[48:49], v[74:75] op_sel_hi:[1,0]
	v_pk_add_f32 v[44:45], v[44:45], v[44:45] op_sel:[0,1] op_sel_hi:[1,0]
	v_pk_mul_f32 v[36:37], v[36:37], v[74:75] op_sel_hi:[1,0]
	v_pk_mul_f32 v[38:39], v[38:39], v[74:75] op_sel_hi:[1,0]
	v_pk_mul_f32 v[40:41], v[40:41], v[74:75] op_sel_hi:[1,0]
	v_pk_mul_f32 v[34:35], v[34:35], v[74:75] op_sel_hi:[1,0]
	v_pk_mul_f32 v[74:75], v[58:59], v[42:43] op_sel_hi:[1,0]
	v_pk_mul_f32 v[78:79], v[60:61], v[42:43] op_sel_hi:[1,0]
	v_pk_mul_f32 v[80:81], v[62:63], v[42:43] op_sel_hi:[1,0]
	v_pk_mul_f32 v[82:83], v[64:65], v[42:43] op_sel_hi:[1,0]
	v_pk_mul_f32 v[92:93], v[52:53], v[42:43] op_sel_hi:[1,0]
	v_mov_b32_e32 v43, v44
	s_nop 1
	v_permlane32_swap_b32_e32 v44, v43
	v_add_f32_e32 v43, v44, v43
	v_rcp_f32_e32 v76, v43
	v_pk_mul_f32 v[96:97], v[54:55], v[42:43] op_sel_hi:[1,0]
	v_pk_mul_f32 v[94:95], v[56:57], v[42:43] op_sel_hi:[1,0]
	v_pk_mul_f32 v[98:99], v[50:51], v[42:43] op_sel_hi:[1,0]
	v_pk_mul_f32 v[100:101], v[4:5], v[76:77] op_sel_hi:[1,0]
	v_pk_mov_b32 v[4:5], v[86:87], v[84:85] op_sel:[1,0]
	v_mov_b32_e32 v87, v85
	v_pk_add_f32 v[4:5], v[4:5], v[86:87]
	v_pk_mul_f32 v[102:103], v[6:7], v[76:77] op_sel_hi:[1,0]
	v_pk_add_f32 v[104:105], v[4:5], v[4:5] op_sel:[0,1] op_sel_hi:[1,0]
	v_cvt_pk_bf16_f32 v7, v40, v41
	ds_read_b128 v[84:87], v150 offset:52224
	ds_read_b128 v[50:53], v150 offset:35840
	ds_read_b128 v[54:57], v150 offset:36864
	ds_read_b128 v[58:61], v150 offset:37888
	ds_read_b128 v[62:65], v150 offset:38912
	v_cvt_pk_bf16_f32 v6, v38, v39
	v_cvt_pk_bf16_f32 v5, v36, v37
	v_cvt_pk_bf16_f32 v4, v34, v35
	ds_read_b128 v[88:91], v150 offset:53248
	ds_read_b128 v[34:37], v150 offset:39936
	ds_read_b128 v[38:41], v150 offset:40960
	ds_read_b128 v[42:45], v150 offset:41984
	ds_read_b128 v[46:49], v150 offset:43008
	v_cvt_pk_bf16_f32 v95, v94, v95
	v_cvt_pk_bf16_f32 v94, v96, v97
	v_cvt_pk_bf16_f32 v93, v92, v93
	v_cvt_pk_bf16_f32 v92, v98, v99
	s_waitcnt lgkmcnt(5)
	v_mfma_f32_32x32x16_bf16 v[50:65], v[84:87], v[4:7], v[50:65]
	v_mul_f32_e32 v10, v10, v76
	v_mul_f32_e32 v11, v11, v76
	v_mul_f32_e32 v12, v12, v76
	v_mul_f32_e32 v13, v13, v76
	v_mul_f32_e32 v8, v8, v76
	v_mul_f32_e32 v9, v9, v76
	v_mov_b32_e32 v77, v104
	s_nop 1
	v_permlane32_swap_b32_e32 v104, v77
	v_cvt_pk_bf16_f32 v73, v72, v73
	s_waitcnt lgkmcnt(0)
	v_mfma_f32_32x32x16_bf16 v[34:49], v[84:87], v[92:95], v[34:49]
	v_cvt_pk_bf16_f32 v72, v70, v71
	v_cvt_pk_bf16_f32 v70, v66, v67
	v_add_f32_e32 v66, v104, v77
	v_cvt_pk_bf16_f32 v71, v68, v69
	v_rcp_f32_e32 v104, v66
	v_cvt_pk_bf16_f32 v69, v82, v83
	v_cvt_pk_bf16_f32 v68, v80, v81
	v_cvt_pk_bf16_f32 v67, v78, v79
	v_cvt_pk_bf16_f32 v66, v74, v75
	ds_read_b128 v[78:81], v150 offset:54272
	v_mfma_f32_32x32x16_bf16 v[50:65], v[88:91], v[70:73], v[50:65]
	v_mul_f32_e32 v2, v2, v76
	v_mul_f32_e32 v3, v3, v76
	v_mul_f32_e32 v20, v20, v104
	v_mul_f32_e32 v21, v21, v104
	v_cvt_pk_bf16_f32 v85, v8, v9
	v_cvt_pk_bf16_f32 v82, v2, v3
	v_pk_mul_f32 v[2:3], v[22:23], v[104:105] op_sel_hi:[1,0]
	v_pk_mul_f32 v[8:9], v[24:25], v[104:105] op_sel_hi:[1,0]
	v_pk_mul_f32 v[18:19], v[18:19], v[104:105] op_sel_hi:[1,0]
	v_mfma_f32_32x32x16_bf16 v[34:49], v[88:91], v[66:69], v[34:49]
	v_cvt_pk_bf16_f32 v84, v102, v103
	v_cvt_pk_bf16_f32 v83, v100, v101
	ds_read_b128 v[86:89], v150 offset:55296
	v_cvt_pk_bf16_f32 v99, v8, v9
	v_cvt_pk_bf16_f32 v98, v2, v3
	v_cvt_pk_bf16_f32 v97, v20, v21
	v_cvt_pk_bf16_f32 v96, v18, v19
	s_waitcnt lgkmcnt(1)
	v_mfma_f32_32x32x16_bf16 v[50:65], v[78:81], v[82:85], v[50:65]
	v_mul_f32_e32 v2, v14, v76
	v_mul_f32_e32 v3, v15, v76
	v_mul_f32_e32 v8, v16, v76
	v_mul_f32_e32 v9, v17, v76
	v_mul_f32_e32 v14, v26, v104
	v_mul_f32_e32 v15, v27, v104
	v_cvt_pk_bf16_f32 v77, v8, v9
	v_cvt_pk_bf16_f32 v76, v2, v3
	v_cvt_pk_bf16_f32 v74, v10, v11
	v_pk_mul_f32 v[2:3], v[28:29], v[104:105] op_sel_hi:[1,0]
	v_mfma_f32_32x32x16_bf16 v[34:49], v[78:81], v[96:99], v[34:49]
	v_mul_f32_e32 v8, v30, v104
	v_mul_f32_e32 v9, v31, v104
	v_mul_f32_e32 v10, v32, v104
	v_mul_f32_e32 v11, v33, v104
	v_cvt_pk_bf16_f32 v75, v12, v13
	v_cvt_pk_bf16_f32 v81, v10, v11
	v_cvt_pk_bf16_f32 v80, v8, v9
	v_cvt_pk_bf16_f32 v79, v2, v3
	v_cvt_pk_bf16_f32 v78, v14, v15
	s_waitcnt lgkmcnt(0)
	v_mfma_f32_32x32x16_bf16 v[50:65], v[86:89], v[74:77], v[50:65]
	v_mfma_f32_32x32x16_bf16 v[34:49], v[86:89], v[78:81], v[34:49]
	ds_read_b128 v[86:89], v150 offset:56320
	ds_read_b128 v[18:21], v150 offset:44032
	ds_read_b128 v[22:25], v150 offset:45056
	ds_read_b128 v[26:29], v150 offset:46080
	ds_read_b128 v[30:33], v150 offset:47104
	ds_read_b128 v[100:103], v150 offset:57344
	s_waitcnt lgkmcnt(1)
	v_mfma_f32_32x32x16_bf16 v[18:33], v[86:89], v[4:7], v[18:33]
	ds_read_b128 v[2:5], v150 offset:48128
	ds_read_b128 v[6:9], v150 offset:49152
	ds_read_b128 v[10:13], v150 offset:50176
	ds_read_b128 v[14:17], v150 offset:51200
	s_waitcnt lgkmcnt(0)
	v_mfma_f32_32x32x16_bf16 v[2:17], v[86:89], v[92:95], v[2:17]
	v_mfma_f32_32x32x16_bf16 v[18:33], v[100:103], v[70:73], v[18:33]
	v_mfma_f32_32x32x16_bf16 v[2:17], v[100:103], v[66:69], v[2:17]
	ds_read_b128 v[66:69], v150 offset:58368
	ds_read_b128 v[70:73], v150 offset:59392
	s_waitcnt lgkmcnt(1)
	v_mfma_f32_32x32x16_bf16 v[18:33], v[66:69], v[82:85], v[18:33]
	v_mfma_f32_32x32x16_bf16 v[2:17], v[66:69], v[96:99], v[2:17]
	s_waitcnt lgkmcnt(0)
	v_mfma_f32_32x32x16_bf16 v[18:33], v[70:73], v[74:77], v[18:33]
	v_mfma_f32_32x32x16_bf16 v[2:17], v[70:73], v[78:81], v[2:17]
	s_nop 10
	v_mul_f32_e32 v66, v22, v22
	v_mul_f32_e32 v67, v23, v23
	v_mul_f32_e32 v68, v30, v30
	v_mul_f32_e32 v69, v31, v31
	v_mul_f32_e32 v70, v24, v24
	v_mul_f32_e32 v71, v25, v25
	v_pk_mul_f32 v[72:73], v[32:33], v[32:33]
	v_pk_mul_f32 v[74:75], v[20:21], v[20:21]
	v_pk_mul_f32 v[76:77], v[28:29], v[28:29]
	v_pk_mul_f32 v[78:79], v[26:27], v[26:27]
	v_pk_mul_f32 v[80:81], v[18:19], v[18:19]
	v_pk_fma_f32 v[78:79], v[58:59], v[58:59], v[78:79]
	v_pk_fma_f32 v[76:77], v[60:61], v[60:61], v[76:77]
	v_pk_fma_f32 v[74:75], v[52:53], v[52:53], v[74:75]
	v_pk_fma_f32 v[72:73], v[64:65], v[64:65], v[72:73]
	v_pk_fma_f32 v[70:71], v[56:57], v[56:57], v[70:71]
	v_pk_fma_f32 v[68:69], v[62:63], v[62:63], v[68:69]
	v_pk_fma_f32 v[66:67], v[54:55], v[54:55], v[66:67]
	v_pk_fma_f32 v[80:81], v[50:51], v[50:51], v[80:81]
	v_pk_add_f32 v[66:67], v[66:67], v[68:69]
	v_pk_add_f32 v[68:69], v[70:71], v[72:73]
	v_pk_add_f32 v[70:71], v[74:75], v[76:77]
	v_pk_add_f32 v[72:73], v[80:81], v[78:79]
	v_pk_add_f32 v[68:69], v[70:71], v[68:69]
	v_pk_add_f32 v[66:67], v[72:73], v[66:67]
	v_pk_mul_f32 v[72:73], v[14:15], v[14:15]
	v_pk_mov_b32 v[70:71], v[66:67], v[68:69] op_sel:[1,0]
	v_mov_b32_e32 v67, v69
	v_pk_add_f32 v[66:67], v[70:71], v[66:67]
	v_pk_mul_f32 v[70:71], v[6:7], v[6:7]
	v_pk_mul_f32 v[74:75], v[8:9], v[8:9]
	v_pk_mul_f32 v[76:77], v[16:17], v[16:17]
	v_pk_mul_f32 v[78:79], v[4:5], v[4:5]
	v_pk_mul_f32 v[80:81], v[12:13], v[12:13]
	v_pk_mul_f32 v[82:83], v[10:11], v[10:11]
	v_pk_mul_f32 v[84:85], v[2:3], v[2:3]
	v_pk_fma_f32 v[82:83], v[42:43], v[42:43], v[82:83]
	v_pk_fma_f32 v[80:81], v[44:45], v[44:45], v[80:81]
	v_pk_fma_f32 v[78:79], v[36:37], v[36:37], v[78:79]
	v_pk_fma_f32 v[76:77], v[48:49], v[48:49], v[76:77]
	v_pk_fma_f32 v[74:75], v[40:41], v[40:41], v[74:75]
	v_pk_fma_f32 v[72:73], v[46:47], v[46:47], v[72:73]
	v_pk_fma_f32 v[70:71], v[38:39], v[38:39], v[70:71]
	v_pk_fma_f32 v[84:85], v[34:35], v[34:35], v[84:85]
	v_pk_add_f32 v[70:71], v[70:71], v[72:73]
	v_pk_add_f32 v[72:73], v[74:75], v[76:77]
	v_pk_add_f32 v[74:75], v[78:79], v[80:81]
	v_pk_add_f32 v[76:77], v[84:85], v[82:83]
	v_pk_add_f32 v[72:73], v[74:75], v[72:73]
	v_pk_add_f32 v[70:71], v[76:77], v[70:71]
	v_pk_add_f32 v[66:67], v[66:67], v[66:67] op_sel:[0,1] op_sel_hi:[1,0]
	v_pk_mov_b32 v[74:75], v[70:71], v[72:73] op_sel:[1,0]
	v_mov_b32_e32 v71, v73
	v_pk_add_f32 v[70:71], v[74:75], v[70:71]
	v_mov_b32_e32 v69, v66
	v_pk_add_f32 v[70:71], v[70:71], v[70:71] op_sel:[0,1] op_sel_hi:[1,0]
	s_nop 0
	v_permlane32_swap_b32_e32 v66, v69
	v_mov_b32_e32 v68, v70
	s_nop 1
	v_permlane32_swap_b32_e32 v70, v68
	v_mov_b32_e32 v71, v66
	v_pk_add_f32 v[66:67], v[70:71], v[68:69]
	v_pk_fma_f32 v[66:67], v[66:67], s[0:1], v[152:153] op_sel_hi:[1,0,0]
	s_mov_b32 s1, 0x800000
	v_mul_f32_e32 v68, 0x4b800000, v67
	v_cmp_gt_f32_e32 vcc, s1, v67
	s_nop 1
	v_cndmask_b32_e32 v67, v67, v68, vcc
	v_rsq_f32_e32 v67, v67
	s_nop 0
	v_mul_f32_e32 v68, 0x45800000, v67
	v_cndmask_b32_e32 v68, v67, v68, vcc
	v_pk_mul_f32 v[158:159], v[50:51], v[68:69] op_sel_hi:[1,0]
	v_pk_mul_f32 v[50:51], v[18:19], v[68:69] op_sel_hi:[1,0]
	v_mul_f32_e32 v18, 0x4b800000, v66
	v_cmp_gt_f32_e32 vcc, s1, v66
	v_pk_mul_f32 v[80:81], v[60:61], v[68:69] op_sel_hi:[1,0]
	v_pk_mul_f32 v[60:61], v[28:29], v[68:69] op_sel_hi:[1,0]
	v_cndmask_b32_e32 v18, v66, v18, vcc
	v_rsq_f32_e32 v18, v18
	v_pk_mul_f32 v[78:79], v[58:59], v[68:69] op_sel_hi:[1,0]
	v_pk_mul_f32 v[160:161], v[52:53], v[68:69] op_sel_hi:[1,0]
	v_pk_mul_f32 v[82:83], v[54:55], v[68:69] op_sel_hi:[1,0]
	v_mul_f32_e32 v19, 0x45800000, v18
	v_cndmask_b32_e32 v28, v18, v19, vcc
	v_pk_mul_f32 v[168:169], v[56:57], v[68:69] op_sel_hi:[1,0]
	v_pk_mul_f32 v[58:59], v[26:27], v[68:69] op_sel_hi:[1,0]
	v_pk_mul_f32 v[52:53], v[20:21], v[68:69] op_sel_hi:[1,0]
	v_pk_mul_f32 v[54:55], v[22:23], v[68:69] op_sel_hi:[1,0]
	v_pk_mul_f32 v[56:57], v[24:25], v[68:69] op_sel_hi:[1,0]
	v_pk_mul_f32 v[18:19], v[42:43], v[28:29] op_sel_hi:[1,0]
	v_pk_mul_f32 v[20:21], v[44:45], v[28:29] op_sel_hi:[1,0]
	v_pk_mul_f32 v[22:23], v[46:47], v[28:29] op_sel_hi:[1,0]
	v_pk_mul_f32 v[26:27], v[48:49], v[28:29] op_sel_hi:[1,0]
	v_pk_mul_f32 v[162:163], v[34:35], v[28:29] op_sel_hi:[1,0]
	v_pk_mul_f32 v[164:165], v[36:37], v[28:29] op_sel_hi:[1,0]
	v_pk_mul_f32 v[166:167], v[38:39], v[28:29] op_sel_hi:[1,0]
	v_pk_mul_f32 v[24:25], v[40:41], v[28:29] op_sel_hi:[1,0]
	v_pk_mul_f32 v[104:105], v[2:3], v[28:29] op_sel_hi:[1,0]
	v_pk_mul_f32 v[112:113], v[4:5], v[28:29] op_sel_hi:[1,0]
	ds_read_b128 v[2:5], v150 offset:60416
	ds_read_b128 v[34:37], v174 offset:32768
	ds_read_b128 v[38:41], v174 offset:32800
	ds_read_b128 v[42:45], v174 offset:32832
	ds_read_b128 v[46:49], v174 offset:32864
	v_cvt_pk_bf16_f32 v129, v168, v169
	v_cvt_pk_bf16_f32 v128, v82, v83
	v_cvt_pk_bf16_f32 v127, v160, v161
	v_cvt_pk_bf16_f32 v126, v158, v159
	v_cvt_pk_bf16_f32 v137, v24, v25
	v_cvt_pk_bf16_f32 v136, v166, v167
	v_cvt_pk_bf16_f32 v135, v164, v165
	s_waitcnt lgkmcnt(0)
	v_mfma_f32_32x32x16_bf16 v[86:101], v[2:5], v[126:129], v[34:49]
	v_cvt_pk_bf16_f32 v134, v162, v163
	v_mul_f32_e32 v84, v62, v68
	v_mul_f32_e32 v85, v63, v68
	v_mul_f32_e32 v170, v64, v68
	v_mul_f32_e32 v171, v65, v68
	v_pk_mul_f32 v[62:63], v[30:31], v[68:69] op_sel_hi:[1,0]
	v_pk_mul_f32 v[64:65], v[32:33], v[68:69] op_sel_hi:[1,0]
	v_pk_mul_f32 v[116:117], v[6:7], v[28:29] op_sel_hi:[1,0]
	v_pk_mul_f32 v[154:155], v[8:9], v[28:29] op_sel_hi:[1,0]
	v_mfma_f32_32x32x16_bf16 v[34:49], v[2:5], v[134:137], v[34:49]
	ds_read_b128 v[6:9], v150 offset:61440
	ds_read_b128 v[66:69], v174 offset:32896
	ds_read_b128 v[106:109], v150 offset:64512
	v_cvt_pk_bf16_f32 v125, v170, v171
	v_cvt_pk_bf16_f32 v124, v84, v85
	v_cvt_pk_bf16_f32 v123, v80, v81
	v_cvt_pk_bf16_f32 v122, v78, v79
	v_cvt_pk_bf16_f32 v149, v26, v27
	v_cvt_pk_bf16_f32 v148, v22, v23
	v_cvt_pk_bf16_f32 v147, v20, v21
	v_cvt_pk_bf16_f32 v146, v18, v19
	s_waitcnt lgkmcnt(2)
	v_mfma_f32_32x32x16_bf16 v[86:101], v[6:9], v[122:125], v[86:101]
	v_mul_f32_e32 v102, v10, v28
	v_mul_f32_e32 v103, v11, v28
	v_mul_f32_e32 v110, v12, v28
	v_mul_f32_e32 v111, v13, v28
	v_mul_f32_e32 v114, v14, v28
	v_mul_f32_e32 v115, v15, v28
	v_pk_mul_f32 v[156:157], v[16:17], v[28:29] op_sel_hi:[1,0]
	ds_read_b128 v[176:179], v174 offset:33536
	ds_read_b128 v[180:183], v174 offset:33568
	ds_read_b128 v[184:187], v174 offset:33600
	ds_read_b128 v[28:31], v174 offset:33632
	ds_read_b128 v[188:191], v174 offset:33792
	ds_read_b128 v[192:195], v174 offset:33824
	ds_read_b128 v[196:199], v174 offset:33856
	ds_read_b128 v[200:203], v174 offset:33888
	ds_read_b128 v[204:207], v150 offset:62464
	v_cvt_pk_bf16_f32 v133, v56, v57
	v_mfma_f32_32x32x16_bf16 v[34:49], v[6:9], v[146:149], v[34:49]
	v_cvt_pk_bf16_f32 v132, v54, v55
	v_cvt_pk_bf16_f32 v131, v52, v53
	v_cvt_pk_bf16_f32 v130, v50, v51
	ds_read_b128 v[70:73], v174 offset:33664
	ds_read_b128 v[74:77], v174 offset:33920
	ds_read_b128 v[208:211], v150 offset:63488
	v_cvt_pk_bf16_f32 v145, v154, v155
	v_cvt_pk_bf16_f32 v144, v116, v117
	v_cvt_pk_bf16_f32 v143, v112, v113
	v_cvt_pk_bf16_f32 v142, v104, v105
	s_waitcnt lgkmcnt(3)
	v_mfma_f32_32x32x16_bf16 v[86:101], v[204:207], v[130:133], v[86:101]
	v_cvt_pk_bf16_f32 v121, v64, v65
	v_cvt_pk_bf16_f32 v120, v62, v63
	v_cvt_pk_bf16_f32 v119, v60, v61
	v_cvt_pk_bf16_f32 v118, v58, v59
	v_cvt_pk_bf16_f32 v141, v156, v157
	v_cvt_pk_bf16_f32 v140, v114, v115
	v_cvt_pk_bf16_f32 v139, v110, v111
	v_mfma_f32_32x32x16_bf16 v[34:49], v[204:207], v[142:145], v[34:49]
	v_cvt_pk_bf16_f32 v138, v102, v103
	v_fma_f32 v16, v30, v170, v202
	v_fma_f32 v17, v31, v171, v203
	v_fma_f32 v14, v28, v84, v200
	v_fma_f32 v15, v29, v85, v201
	v_pk_fma_f32 v[12:13], v[186:187], v[80:81], v[198:199]
	v_pk_fma_f32 v[10:11], v[184:185], v[78:79], v[196:197]
	v_pk_fma_f32 v[8:9], v[182:183], v[168:169], v[194:195]
	s_waitcnt lgkmcnt(0)
	v_mfma_f32_32x32x16_bf16 v[86:101], v[208:211], v[118:121], v[86:101]
	v_fma_f32 v6, v180, v82, v192
	v_fma_f32 v7, v181, v83, v193
	ds_read_b128 v[78:81], v174 offset:33760
	ds_read_b128 v[82:85], v174 offset:33248
	v_fma_f32 v4, v178, v160, v190
	v_fma_f32 v5, v179, v161, v191
	v_pk_fma_f32 v[2:3], v[176:177], v[158:159], v[188:189]
	v_pk_fma_f32 v[32:33], v[30:31], v[26:27], v[202:203]
	v_pk_fma_f32 v[30:31], v[28:29], v[22:23], v[200:201]
	v_pk_fma_f32 v[28:29], v[186:187], v[20:21], v[198:199]
	v_pk_fma_f32 v[26:27], v[184:185], v[18:19], v[196:197]
	v_pk_fma_f32 v[24:25], v[182:183], v[24:25], v[194:195]
	v_pk_fma_f32 v[22:23], v[180:181], v[166:167], v[192:193]
	v_pk_fma_f32 v[20:21], v[178:179], v[164:165], v[190:191]
	v_pk_fma_f32 v[18:19], v[176:177], v[162:163], v[188:189]
	ds_read_b128 v[158:161], v174 offset:33696
	ds_read_b128 v[162:165], v174 offset:33728
	ds_read_b128 v[166:169], v174 offset:33952
	ds_read_b128 v[176:179], v174 offset:33984
	ds_read_b128 v[180:183], v174 offset:34016
	ds_read_b128 v[184:187], v212 offset:11264
	v_mfma_f32_32x32x16_bf16 v[34:49], v[208:211], v[138:141], v[34:49]
	v_cvt_pk_bf16_f32 v86, v86, v87
	v_cvt_pk_bf16_f32 v87, v88, v89
	v_cvt_pk_bf16_f32 v88, v90, v91
	v_cvt_pk_bf16_f32 v89, v92, v93
	ds_read_b128 v[90:93], v212 offset:12288
	v_pk_max_i16 v86, v86, 0
	v_pk_max_i16 v87, v87, 0
	v_pk_max_i16 v88, v88, 0
	v_pk_max_i16 v89, v89, 0
	s_nop 1
	s_nop 0
	v_cvt_pk_bf16_f32 v188, v34, v35
	v_cvt_pk_bf16_f32 v189, v36, v37
	v_cvt_pk_bf16_f32 v190, v38, v39
	v_cvt_pk_bf16_f32 v191, v40, v41
	s_waitcnt lgkmcnt(1)
	v_mfma_f32_32x32x16_bf16 v[2:17], v[184:187], v[86:89], v[2:17]
	v_pk_max_i16 v188, v188, 0
	v_pk_max_i16 v189, v189, 0
	v_pk_max_i16 v190, v190, 0
	v_pk_max_i16 v191, v191, 0
	v_cvt_pk_bf16_f32 v94, v94, v95
	v_cvt_pk_bf16_f32 v95, v96, v97
	v_cvt_pk_bf16_f32 v96, v98, v99
	v_cvt_pk_bf16_f32 v97, v100, v101
	v_cvt_pk_bf16_f32 v98, v42, v43
	v_cvt_pk_bf16_f32 v99, v44, v45
	v_mfma_f32_32x32x16_bf16 v[18:33], v[184:187], v[188:191], v[18:33]
	ds_read_b128 v[184:187], v212 offset:19456
	v_cvt_pk_bf16_f32 v100, v46, v47
	v_cvt_pk_bf16_f32 v101, v48, v49
	v_fma_f32 v64, v80, v64, v182
	v_fma_f32 v65, v81, v65, v183
	v_pk_fma_f32 v[62:63], v[78:79], v[62:63], v[180:181]
	v_pk_fma_f32 v[60:61], v[164:165], v[60:61], v[178:179]
	v_pk_fma_f32 v[58:59], v[162:163], v[58:59], v[176:177]
	v_pk_max_i16 v94, v94, 0
	v_pk_max_i16 v95, v95, 0
	v_pk_max_i16 v96, v96, 0
	v_pk_max_i16 v97, v97, 0
	v_pk_max_i16 v98, v98, 0
	v_pk_max_i16 v99, v99, 0
	v_pk_max_i16 v100, v100, 0
	v_pk_max_i16 v101, v101, 0
	v_pk_fma_f32 v[56:57], v[160:161], v[56:57], v[168:169]
	s_waitcnt lgkmcnt(1)
	v_mfma_f32_32x32x16_bf16 v[2:17], v[90:93], v[94:97], v[2:17]
	v_fma_f32 v54, v158, v54, v166
	v_fma_f32 v55, v159, v55, v167
	v_fma_f32 v52, v72, v52, v76
	v_fma_f32 v53, v73, v53, v77
	v_fma_f32 v50, v70, v50, v74
	v_fma_f32 v51, v71, v51, v75
	v_pk_fma_f32 v[48:49], v[80:81], v[156:157], v[182:183]
	v_pk_fma_f32 v[46:47], v[78:79], v[114:115], v[180:181]
	v_pk_fma_f32 v[44:45], v[164:165], v[110:111], v[178:179]
	v_pk_fma_f32 v[42:43], v[162:163], v[102:103], v[176:177]
	v_mfma_f32_32x32x16_bf16 v[18:33], v[90:93], v[98:101], v[18:33]
	ds_read_b128 v[90:93], v212 offset:20480
	v_fma_f32 v40, v160, v154, v168
	v_fma_f32 v41, v161, v155, v169
	v_fma_f32 v38, v158, v116, v166
	v_fma_f32 v39, v159, v117, v167
	v_pk_fma_f32 v[36:37], v[72:73], v[112:113], v[76:77]
	v_pk_fma_f32 v[34:35], v[70:71], v[104:105], v[74:75]
	s_waitcnt lgkmcnt(1)
	v_mfma_f32_32x32x16_bf16 v[50:65], v[184:187], v[86:89], v[50:65]
	ds_read_b128 v[70:73], v174 offset:32928
	ds_read_b128 v[74:77], v174 offset:32960
	ds_read_b128 v[78:81], v174 offset:32992
	ds_read_b128 v[86:89], v174 offset:33024
	ds_read_b128 v[110:113], v212 offset:1024
	v_mfma_f32_32x32x16_bf16 v[34:49], v[184:187], v[188:191], v[34:49]
	s_waitcnt lgkmcnt(5)
	v_mfma_f32_32x32x16_bf16 v[50:65], v[90:93], v[94:97], v[50:65]
	v_mfma_f32_32x32x16_bf16 v[34:49], v[90:93], v[98:101], v[34:49]
	s_waitcnt lgkmcnt(2)
	v_mfma_f32_32x32x16_bf16 v[90:105], v[106:109], v[126:129], v[66:81]
	v_mfma_f32_32x32x16_bf16 v[66:81], v[106:109], v[134:137], v[66:81]
	ds_read_b128 v[106:109], v212 offset:0
	s_waitcnt lgkmcnt(0)
	v_mfma_f32_32x32x16_bf16 v[90:105], v[106:109], v[122:125], v[90:105]
	v_mfma_f32_32x32x16_bf16 v[66:81], v[106:109], v[146:149], v[66:81]
	ds_read_b128 v[106:109], v212 offset:2048
	v_mfma_f32_32x32x16_bf16 v[90:105], v[110:113], v[130:133], v[90:105]
	v_mfma_f32_32x32x16_bf16 v[66:81], v[110:113], v[142:145], v[66:81]
	ds_read_b128 v[110:113], v212 offset:13312
	s_waitcnt lgkmcnt(1)
	v_mfma_f32_32x32x16_bf16 v[90:105], v[106:109], v[118:121], v[90:105]
	v_mfma_f32_32x32x16_bf16 v[66:81], v[106:109], v[138:141], v[66:81]
	s_nop 10
	v_cvt_pk_bf16_f32 v90, v90, v91
	v_cvt_pk_bf16_f32 v91, v92, v93
	v_cvt_pk_bf16_f32 v92, v94, v95
	v_cvt_pk_bf16_f32 v94, v98, v99
	v_cvt_pk_bf16_f32 v95, v100, v101
	ds_read_b128 v[98:101], v212 offset:21504
	v_cvt_pk_bf16_f32 v66, v66, v67
	v_cvt_pk_bf16_f32 v67, v68, v69
	v_cvt_pk_bf16_f32 v68, v70, v71
	v_cvt_pk_bf16_f32 v93, v96, v97
	v_cvt_pk_bf16_f32 v69, v72, v73
	ds_read_b128 v[70:73], v212 offset:14336
	v_pk_max_i16 v90, v90, 0
	v_pk_max_i16 v91, v91, 0
	v_pk_max_i16 v92, v92, 0
	v_pk_max_i16 v93, v93, 0
	v_pk_max_i16 v66, v66, 0
	v_pk_max_i16 v67, v67, 0
	v_pk_max_i16 v68, v68, 0
	v_pk_max_i16 v69, v69, 0
	v_cvt_pk_bf16_f32 v96, v102, v103
	s_waitcnt lgkmcnt(2)
	v_mfma_f32_32x32x16_bf16 v[2:17], v[110:113], v[90:93], v[2:17]
	v_cvt_pk_bf16_f32 v97, v104, v105
	v_cvt_pk_bf16_f32 v74, v74, v75
	v_cvt_pk_bf16_f32 v75, v76, v77
	v_cvt_pk_bf16_f32 v76, v78, v79
	v_cvt_pk_bf16_f32 v77, v80, v81
	v_pk_max_i16 v94, v94, 0
	v_pk_max_i16 v95, v95, 0
	v_pk_max_i16 v96, v96, 0
	v_pk_max_i16 v97, v97, 0
	v_pk_max_i16 v74, v74, 0
	v_pk_max_i16 v75, v75, 0
	v_pk_max_i16 v76, v76, 0
	v_pk_max_i16 v77, v77, 0
	v_mfma_f32_32x32x16_bf16 v[18:33], v[110:113], v[66:69], v[18:33]
	s_waitcnt lgkmcnt(1)
	v_mfma_f32_32x32x16_bf16 v[34:49], v[98:101], v[66:69], v[34:49]
	ds_read_b128 v[66:69], v212 offset:22528
	v_mfma_f32_32x32x16_bf16 v[50:65], v[98:101], v[90:93], v[50:65]
	s_waitcnt lgkmcnt(1)
	v_mfma_f32_32x32x16_bf16 v[2:17], v[70:73], v[94:97], v[2:17]
	v_mfma_f32_32x32x16_bf16 v[18:33], v[70:73], v[74:77], v[18:33]
	ds_read_b128 v[78:81], v212 offset:3072
	s_waitcnt lgkmcnt(1)
	v_mfma_f32_32x32x16_bf16 v[50:65], v[66:69], v[94:97], v[50:65]
	ds_read_b128 v[90:93], v174 offset:33056
	ds_read_b128 v[94:97], v174 offset:33088
	ds_read_b128 v[98:101], v174 offset:33120
	ds_read_b128 v[70:73], v174 offset:33152
	v_mfma_f32_32x32x16_bf16 v[34:49], v[66:69], v[74:77], v[34:49]
	ds_read_b128 v[66:69], v212 offset:4096
	ds_read_b128 v[74:77], v212 offset:5120
	s_waitcnt lgkmcnt(3)
	v_mfma_f32_32x32x16_bf16 v[102:117], v[78:81], v[126:129], v[86:101]
	v_mfma_f32_32x32x16_bf16 v[86:101], v[78:81], v[134:137], v[86:101]
	s_waitcnt lgkmcnt(1)
	v_mfma_f32_32x32x16_bf16 v[86:101], v[66:69], v[146:149], v[86:101]
	v_mfma_f32_32x32x16_bf16 v[102:117], v[66:69], v[122:125], v[102:117]
	ds_read_b128 v[66:69], v212 offset:6144
	s_waitcnt lgkmcnt(1)
	v_mfma_f32_32x32x16_bf16 v[86:101], v[74:77], v[142:145], v[86:101]
	v_mfma_f32_32x32x16_bf16 v[102:117], v[74:77], v[130:133], v[102:117]
	ds_read_b128 v[74:77], v212 offset:15360
	s_waitcnt lgkmcnt(1)
	v_mfma_f32_32x32x16_bf16 v[86:101], v[66:69], v[138:141], v[86:101]
	v_mfma_f32_32x32x16_bf16 v[102:117], v[66:69], v[118:121], v[102:117]
	s_nop 10
	v_cvt_pk_bf16_f32 v78, v86, v87
	v_cvt_pk_bf16_f32 v80, v90, v91
	v_cvt_pk_bf16_f32 v79, v88, v89
	v_cvt_pk_bf16_f32 v81, v92, v93
	ds_read_b128 v[86:89], v212 offset:16384
	ds_read_b128 v[90:93], v212 offset:23552
	v_cvt_pk_bf16_f32 v66, v102, v103
	v_cvt_pk_bf16_f32 v67, v104, v105
	v_cvt_pk_bf16_f32 v68, v106, v107
	v_cvt_pk_bf16_f32 v69, v108, v109
	v_pk_max_i16 v66, v66, 0
	v_pk_max_i16 v67, v67, 0
	v_pk_max_i16 v68, v68, 0
	v_pk_max_i16 v69, v69, 0
	v_pk_max_i16 v78, v78, 0
	v_pk_max_i16 v79, v79, 0
	v_pk_max_i16 v80, v80, 0
	v_pk_max_i16 v81, v81, 0
	v_cvt_pk_bf16_f32 v94, v94, v95
	s_waitcnt lgkmcnt(2)
	v_mfma_f32_32x32x16_bf16 v[18:33], v[74:77], v[78:81], v[18:33]
	v_cvt_pk_bf16_f32 v95, v96, v97
	v_cvt_pk_bf16_f32 v96, v98, v99
	v_cvt_pk_bf16_f32 v97, v100, v101
	v_pk_max_i16 v94, v94, 0
	v_pk_max_i16 v95, v95, 0
	v_pk_max_i16 v96, v96, 0
	v_pk_max_i16 v97, v97, 0
	v_mfma_f32_32x32x16_bf16 v[2:17], v[74:77], v[66:69], v[2:17]
	v_cvt_pk_bf16_f32 v74, v110, v111
	v_cvt_pk_bf16_f32 v75, v112, v113
	v_cvt_pk_bf16_f32 v76, v114, v115
	v_cvt_pk_bf16_f32 v77, v116, v117
	v_pk_max_i16 v74, v74, 0
	v_pk_max_i16 v75, v75, 0
	v_pk_max_i16 v76, v76, 0
	v_pk_max_i16 v77, v77, 0
	s_waitcnt lgkmcnt(0)
	v_mfma_f32_32x32x16_bf16 v[50:65], v[90:93], v[66:69], v[50:65]
	ds_read_b128 v[66:69], v212 offset:24576
	v_mfma_f32_32x32x16_bf16 v[34:49], v[90:93], v[78:81], v[34:49]
	ds_read_b128 v[102:105], v212 offset:7168
	v_mfma_f32_32x32x16_bf16 v[2:17], v[86:89], v[74:77], v[2:17]
	s_waitcnt lgkmcnt(1)
	v_mfma_f32_32x32x16_bf16 v[50:65], v[66:69], v[74:77], v[50:65]
	ds_read_b128 v[74:77], v174 offset:33184
	ds_read_b128 v[78:81], v174 offset:33216
	v_mfma_f32_32x32x16_bf16 v[34:49], v[66:69], v[94:97], v[34:49]
	ds_read_b128 v[66:69], v212 offset:8192
	v_mfma_f32_32x32x16_bf16 v[18:33], v[86:89], v[94:97], v[18:33]
	s_waitcnt lgkmcnt(1)
	v_mfma_f32_32x32x16_bf16 v[86:101], v[102:105], v[126:129], v[70:85]
	v_mfma_f32_32x32x16_bf16 v[70:85], v[102:105], v[134:137], v[70:85]
	ds_read_b128 v[102:105], v212 offset:9216
	v_lshlrev_b32_e32 v135, 2, v1
	v_add_u32_e32 v134, v172, v174
	s_waitcnt lgkmcnt(1)
	v_mfma_f32_32x32x16_bf16 v[86:101], v[66:69], v[122:125], v[86:101]
	v_mfma_f32_32x32x16_bf16 v[70:85], v[66:69], v[146:149], v[70:85]
	ds_read_b128 v[66:69], v212 offset:10240
	s_waitcnt lgkmcnt(1)
	v_mfma_f32_32x32x16_bf16 v[86:101], v[102:105], v[130:133], v[86:101]
	v_mfma_f32_32x32x16_bf16 v[70:85], v[102:105], v[142:145], v[70:85]
	ds_read_b128 v[102:105], v212 offset:17408
	s_waitcnt lgkmcnt(1)
	v_mfma_f32_32x32x16_bf16 v[86:101], v[66:69], v[118:121], v[86:101]
	v_mfma_f32_32x32x16_bf16 v[70:85], v[66:69], v[138:141], v[70:85]
	s_nop 10
	v_cvt_pk_bf16_f32 v68, v90, v91
	v_cvt_pk_bf16_f32 v69, v92, v93
	ds_read_b128 v[90:93], v212 offset:25600
	v_cvt_pk_bf16_f32 v66, v86, v87
	v_cvt_pk_bf16_f32 v67, v88, v89
	v_pk_max_i16 v66, v66, 0
	v_pk_max_i16 v67, v67, 0
	v_pk_max_i16 v68, v68, 0
	v_pk_max_i16 v69, v69, 0
	v_cvt_pk_bf16_f32 v70, v70, v71
	v_cvt_pk_bf16_f32 v71, v72, v73
	s_waitcnt lgkmcnt(1)
	v_mfma_f32_32x32x16_bf16 v[2:17], v[102:105], v[66:69], v[2:17]
	v_cvt_pk_bf16_f32 v72, v74, v75
	v_cvt_pk_bf16_f32 v73, v76, v77
	ds_read_b128 v[74:77], v212 offset:18432
	v_cvt_pk_bf16_f32 v86, v94, v95
	v_cvt_pk_bf16_f32 v87, v96, v97
	v_cvt_pk_bf16_f32 v88, v98, v99
	s_waitcnt lgkmcnt(1)
	v_mfma_f32_32x32x16_bf16 v[50:65], v[90:93], v[66:69], v[50:65]
	ds_read_b128 v[66:69], v212 offset:26624
	v_cvt_pk_bf16_f32 v89, v100, v101
	v_pk_max_i16 v86, v86, 0
	v_pk_max_i16 v87, v87, 0
	v_pk_max_i16 v88, v88, 0
	v_pk_max_i16 v89, v89, 0
	v_pk_max_i16 v70, v70, 0
	v_pk_max_i16 v71, v71, 0
	v_pk_max_i16 v72, v72, 0
	v_pk_max_i16 v73, v73, 0
	v_cvt_pk_bf16_f32 v78, v78, v79
	v_cvt_pk_bf16_f32 v79, v80, v81
	s_waitcnt lgkmcnt(1)
	v_mfma_f32_32x32x16_bf16 v[2:17], v[74:77], v[86:89], v[2:17]
	v_cvt_pk_bf16_f32 v80, v82, v83
	v_cvt_pk_bf16_f32 v81, v84, v85
	v_pk_max_i16 v78, v78, 0
	v_pk_max_i16 v79, v79, 0
	v_pk_max_i16 v80, v80, 0
	v_pk_max_i16 v81, v81, 0
	s_waitcnt lgkmcnt(0)
	v_mfma_f32_32x32x16_bf16 v[50:65], v[66:69], v[86:89], v[50:65]
	v_mfma_f32_32x32x16_bf16 v[34:49], v[90:93], v[70:73], v[34:49]
	s_nop 10
	v_add_f32_e32 v130, v10, v58
	v_add_f32_e32 v131, v11, v59
	v_add_f32_e32 v132, v12, v60
	v_add_f32_e32 v133, v13, v61
	v_add_f32_e32 v138, v4, v52
	v_add_f32_e32 v139, v5, v53
	v_pk_add_f32 v[140:141], v[16:17], v[64:65]
	v_pk_add_f32 v[142:143], v[8:9], v[56:57]
	v_pk_add_f32 v[144:145], v[14:15], v[62:63]
	v_pk_add_f32 v[146:147], v[6:7], v[54:55]
	v_mfma_f32_32x32x16_bf16 v[18:33], v[102:105], v[70:73], v[18:33]
	ds_read2st64_b32 v[70:71], v135 offset0:133 offset1:134
	v_add_f32_e32 v148, v2, v50
	v_add_f32_e32 v149, v3, v51
	v_add_f32_e32 v144, v146, v144
	v_add_f32_e32 v145, v147, v145
	v_pk_add_f32 v[140:141], v[142:143], v[140:141]
	v_pk_add_f32 v[132:133], v[138:139], v[132:133]
	v_pk_add_f32 v[130:131], v[148:149], v[130:131]
	v_pk_add_f32 v[132:133], v[132:133], v[140:141]
	v_pk_add_f32 v[130:131], v[130:131], v[144:145]
	v_mfma_f32_32x32x16_bf16 v[34:49], v[66:69], v[78:81], v[34:49]
	v_pk_mov_b32 v[138:139], v[130:131], v[132:133] op_sel:[1,0]
	v_mov_b32_e32 v131, v133
	s_waitcnt vmcnt(0) lgkmcnt(0)
	v_mul_f32_e32 v66, v175, v70
	v_pk_add_f32 v[130:131], v[138:139], v[130:131]
	ds_write_b32 v173, v66 offset:512
	v_mul_f32_e32 v66, v175, v71
	v_pk_add_f32 v[130:131], v[130:131], v[130:131] op_sel:[0,1] op_sel_hi:[1,0]
	s_waitcnt lgkmcnt(0)
	ds_read_b128 v[102:105], v174 offset:34560
	ds_read_b128 v[98:101], v174 offset:34592
	ds_read_b128 v[110:113], v174 offset:34624
	ds_read_b128 v[106:109], v174 offset:34656
	ds_read_b128 v[114:117], v174 offset:34688
	ds_read_b128 v[122:125], v174 offset:34720
	ds_read_b128 v[118:121], v174 offset:34752
	ds_read_b128 v[126:129], v174 offset:34784
	v_mov_b32_dpp v66, v66 quad_perm:[1,0,3,2] row_mask:0xf bank_mask:0xf bound_ctrl:1
	v_mov_b32_e32 v131, v130
	v_fmac_f32_e32 v66, v175, v71
	s_nop 0
	v_permlane32_swap_b32_e32 v130, v131
	v_add_f32_dpp v66, v66, v66 quad_perm:[2,3,0,1] row_mask:0xf bank_mask:0xf bound_ctrl:1
	v_add_f32_e32 v130, v130, v131
	v_fmamk_f32 v65, v130, 0xbc800000, v65
	v_add_f32_dpp v66, v66, v66 row_half_mirror row_mask:0xf bank_mask:0xf bound_ctrl:1
	v_fmamk_f32 v64, v130, 0xbc800000, v64
	v_fmamk_f32 v63, v130, 0xbc800000, v63
	v_fmamk_f32 v62, v130, 0xbc800000, v62
	v_fmamk_f32 v61, v130, 0xbc800000, v61
	v_fmamk_f32 v60, v130, 0xbc800000, v60
	v_fmamk_f32 v59, v130, 0xbc800000, v59
	v_fmamk_f32 v58, v130, 0xbc800000, v58
	v_fmamk_f32 v57, v130, 0xbc800000, v57
	v_fmamk_f32 v56, v130, 0xbc800000, v56
	v_fmamk_f32 v55, v130, 0xbc800000, v55
	v_fmamk_f32 v54, v130, 0xbc800000, v54
	v_fmamk_f32 v53, v130, 0xbc800000, v53
	v_fmamk_f32 v52, v130, 0xbc800000, v52
	v_fmamk_f32 v51, v130, 0xbc800000, v51
	v_fmac_f32_e32 v50, 0xbc800000, v130
	v_add_f32_dpp v66, v66, v66 row_ror:8 row_mask:0xf bank_mask:0xf bound_ctrl:1
	v_fmamk_f32 v17, v130, 0xbc800000, v17
	v_fmamk_f32 v16, v130, 0xbc800000, v16
	v_fmamk_f32 v15, v130, 0xbc800000, v15
	v_fmamk_f32 v14, v130, 0xbc800000, v14
	v_fmamk_f32 v13, v130, 0xbc800000, v13
	v_fmamk_f32 v12, v130, 0xbc800000, v12
	v_fmamk_f32 v11, v130, 0xbc800000, v11
	v_fmamk_f32 v10, v130, 0xbc800000, v10
	v_fmamk_f32 v9, v130, 0xbc800000, v9
	v_fmamk_f32 v8, v130, 0xbc800000, v8
	v_fmamk_f32 v7, v130, 0xbc800000, v7
	v_fmamk_f32 v6, v130, 0xbc800000, v6
	v_fmamk_f32 v5, v130, 0xbc800000, v5
	v_fmamk_f32 v4, v130, 0xbc800000, v4
	v_fmamk_f32 v3, v130, 0xbc800000, v3
	v_fmac_f32_e32 v2, 0xbc800000, v130
	v_pk_mul_f32 v[130:131], v[54:55], v[54:55]
	v_pk_mul_f32 v[132:133], v[62:63], v[62:63]
	v_pk_mul_f32 v[138:139], v[50:51], v[50:51]
	v_pk_mul_f32 v[140:141], v[58:59], v[58:59]
	v_pk_mul_f32 v[142:143], v[56:57], v[56:57]
	v_pk_mul_f32 v[144:145], v[64:65], v[64:65]
	v_pk_mul_f32 v[146:147], v[52:53], v[52:53]
	v_pk_mul_f32 v[148:149], v[60:61], v[60:61]
	v_mov_b32_e32 v67, v66
	v_pk_fma_f32 v[148:149], v[12:13], v[12:13], v[148:149]
	v_pk_fma_f32 v[146:147], v[4:5], v[4:5], v[146:147]
	v_pk_fma_f32 v[144:145], v[16:17], v[16:17], v[144:145]
	v_pk_fma_f32 v[142:143], v[8:9], v[8:9], v[142:143]
	v_pk_fma_f32 v[140:141], v[10:11], v[10:11], v[140:141]
	v_pk_fma_f32 v[138:139], v[2:3], v[2:3], v[138:139]
	v_pk_fma_f32 v[132:133], v[14:15], v[14:15], v[132:133]
	v_pk_fma_f32 v[130:131], v[6:7], v[6:7], v[130:131]
	v_permlane16_swap_b32_e32 v66, v67
	v_pk_add_f32 v[130:131], v[130:131], v[132:133]
	v_pk_add_f32 v[132:133], v[138:139], v[140:141]
	v_pk_add_f32 v[138:139], v[142:143], v[144:145]
	v_pk_add_f32 v[140:141], v[146:147], v[148:149]
	v_mfma_f32_32x32x16_bf16 v[18:33], v[74:77], v[78:81], v[18:33]
	v_add_f32_e32 v136, v66, v67
	ds_read_b128 v[70:73], v134 offset:512
	ds_read_b128 v[66:69], v134 offset:544
	ds_read_b128 v[78:81], v134 offset:576
	ds_read_b128 v[74:77], v134 offset:608
	ds_read_b128 v[82:85], v134 offset:640
	ds_read_b128 v[90:93], v134 offset:672
	ds_read_b128 v[86:89], v134 offset:704
	ds_read_b128 v[94:97], v134 offset:736
	v_pk_add_f32 v[138:139], v[140:141], v[138:139]
	v_pk_add_f32 v[130:131], v[132:133], v[130:131]
	s_waitcnt lgkmcnt(8)
	v_pk_mul_f32 v[140:141], v[126:127], v[62:63]
	v_pk_mov_b32 v[132:133], v[130:131], v[138:139] op_sel:[1,0]
	v_mov_b32_e32 v131, v139
	v_pk_mul_f32 v[138:139], v[122:123], v[54:55]
	v_pk_mul_f32 v[142:143], v[114:115], v[50:51]
	v_pk_mul_f32 v[144:145], v[118:119], v[58:59]
	v_pk_mul_f32 v[146:147], v[124:125], v[56:57]
	v_pk_mul_f32 v[148:149], v[128:129], v[64:65]
	v_pk_mul_f32 v[154:155], v[116:117], v[52:53]
	v_pk_mul_f32 v[156:157], v[120:121], v[60:61]
	v_pk_fma_f32 v[154:155], v[104:105], v[4:5], v[154:155]
	v_pk_fma_f32 v[156:157], v[112:113], v[12:13], v[156:157]
	v_pk_fma_f32 v[148:149], v[108:109], v[16:17], v[148:149]
	v_pk_fma_f32 v[146:147], v[100:101], v[8:9], v[146:147]
	v_pk_fma_f32 v[144:145], v[110:111], v[10:11], v[144:145]
	v_pk_fma_f32 v[142:143], v[102:103], v[2:3], v[142:143]
	v_pk_fma_f32 v[140:141], v[106:107], v[14:15], v[140:141]
	v_pk_fma_f32 v[138:139], v[98:99], v[6:7], v[138:139]
	v_pk_add_f32 v[130:131], v[132:133], v[130:131]
	v_pk_add_f32 v[138:139], v[138:139], v[140:141]
	v_pk_add_f32 v[140:141], v[142:143], v[144:145]
	v_pk_add_f32 v[142:143], v[146:147], v[148:149]
	v_pk_add_f32 v[144:145], v[154:155], v[156:157]
	v_pk_add_f32 v[132:133], v[130:131], v[130:131] op_sel:[0,1] op_sel_hi:[1,0]
	v_pk_add_f32 v[142:143], v[144:145], v[142:143]
	v_pk_add_f32 v[138:139], v[140:141], v[138:139]
	v_add_f32_e32 v133, v142, v143
	v_add_f32_e32 v130, v138, v139
	s_waitcnt lgkmcnt(2)
	v_pk_mul_f32 v[138:139], v[90:91], v[54:55]
	s_waitcnt lgkmcnt(0)
	v_pk_mul_f32 v[140:141], v[94:95], v[62:63]
	v_pk_mul_f32 v[142:143], v[82:83], v[50:51]
	v_pk_mul_f32 v[144:145], v[86:87], v[58:59]
	v_pk_mul_f32 v[146:147], v[92:93], v[56:57]
	v_pk_mul_f32 v[148:149], v[96:97], v[64:65]
	v_pk_mul_f32 v[154:155], v[84:85], v[52:53]
	v_pk_mul_f32 v[156:157], v[88:89], v[60:61]
	v_add_f32_e32 v130, v130, v133
	v_pk_fma_f32 v[156:157], v[80:81], v[12:13], v[156:157]
	v_pk_fma_f32 v[154:155], v[72:73], v[4:5], v[154:155]
	v_pk_fma_f32 v[148:149], v[76:77], v[16:17], v[148:149]
	v_pk_fma_f32 v[146:147], v[68:69], v[8:9], v[146:147]
	v_pk_fma_f32 v[144:145], v[78:79], v[10:11], v[144:145]
	v_pk_fma_f32 v[142:143], v[70:71], v[2:3], v[142:143]
	v_pk_fma_f32 v[140:141], v[74:75], v[14:15], v[140:141]
	v_pk_fma_f32 v[138:139], v[66:67], v[6:7], v[138:139]
	v_mov_b32_e32 v133, v130
	v_pk_add_f32 v[138:139], v[138:139], v[140:141]
	v_pk_add_f32 v[140:141], v[142:143], v[144:145]
	v_pk_add_f32 v[142:143], v[146:147], v[148:149]
	v_pk_add_f32 v[144:145], v[154:155], v[156:157]
	v_permlane32_swap_b32_e32 v130, v133
	v_pk_add_f32 v[142:143], v[144:145], v[142:143]
	v_add_f32_e32 v160, v130, v133
	v_pk_add_f32 v[138:139], v[140:141], v[138:139]
	v_add_f32_e32 v133, v142, v143
	v_pk_add_f32 v[140:141], v[26:27], v[42:43]
	v_pk_add_f32 v[142:143], v[28:29], v[44:45]
	v_pk_add_f32 v[144:145], v[20:21], v[36:37]
	v_pk_add_f32 v[146:147], v[32:33], v[48:49]
	v_pk_add_f32 v[148:149], v[24:25], v[40:41]
	v_pk_add_f32 v[154:155], v[30:31], v[46:47]
	v_pk_add_f32 v[156:157], v[22:23], v[38:39]
	v_pk_add_f32 v[158:159], v[18:19], v[34:35]
	v_pk_add_f32 v[154:155], v[156:157], v[154:155]
	v_pk_add_f32 v[146:147], v[148:149], v[146:147]
	v_pk_add_f32 v[142:143], v[144:145], v[142:143]
	v_pk_add_f32 v[140:141], v[158:159], v[140:141]
	v_pk_add_f32 v[142:143], v[142:143], v[146:147]
	v_pk_add_f32 v[140:141], v[140:141], v[154:155]
	v_add_f32_e32 v130, v138, v139
	v_pk_mov_b32 v[144:145], v[140:141], v[142:143] op_sel:[1,0]
	v_mov_b32_e32 v141, v143
	v_pk_add_f32 v[140:141], v[144:145], v[140:141]
	v_add_f32_e32 v133, v130, v133
	v_pk_add_f32 v[140:141], v[140:141], v[140:141] op_sel:[0,1] op_sel_hi:[1,0]
	v_mov_b32_e32 v131, v132
	v_mov_b32_e32 v130, v140
	s_nop 1
	v_permlane32_swap_b32_e32 v140, v130
	v_add_f32_e32 v130, v140, v130
	v_fmamk_f32 v49, v130, 0xbc800000, v49
	v_fmamk_f32 v48, v130, 0xbc800000, v48
	v_fmamk_f32 v47, v130, 0xbc800000, v47
	v_fmamk_f32 v46, v130, 0xbc800000, v46
	v_fmamk_f32 v45, v130, 0xbc800000, v45
	v_fmamk_f32 v44, v130, 0xbc800000, v44
	v_fmamk_f32 v43, v130, 0xbc800000, v43
	v_fmamk_f32 v42, v130, 0xbc800000, v42
	v_fmamk_f32 v41, v130, 0xbc800000, v41
	v_fmamk_f32 v40, v130, 0xbc800000, v40
	v_fmamk_f32 v39, v130, 0xbc800000, v39
	v_fmamk_f32 v38, v130, 0xbc800000, v38
	v_fmamk_f32 v37, v130, 0xbc800000, v37
	v_fmamk_f32 v36, v130, 0xbc800000, v36
	v_fmamk_f32 v35, v130, 0xbc800000, v35
	v_fmac_f32_e32 v34, 0xbc800000, v130
	v_fmamk_f32 v33, v130, 0xbc800000, v33
	v_fmamk_f32 v32, v130, 0xbc800000, v32
	v_fmamk_f32 v31, v130, 0xbc800000, v31
	v_fmamk_f32 v30, v130, 0xbc800000, v30
	v_fmamk_f32 v29, v130, 0xbc800000, v29
	v_fmamk_f32 v28, v130, 0xbc800000, v28
	v_fmamk_f32 v27, v130, 0xbc800000, v27
	v_fmamk_f32 v26, v130, 0xbc800000, v26
	v_fmamk_f32 v25, v130, 0xbc800000, v25
	v_fmamk_f32 v24, v130, 0xbc800000, v24
	v_fmamk_f32 v23, v130, 0xbc800000, v23
	v_fmamk_f32 v22, v130, 0xbc800000, v22
	v_fmamk_f32 v21, v130, 0xbc800000, v21
	v_fmamk_f32 v20, v130, 0xbc800000, v20
	v_fmamk_f32 v19, v130, 0xbc800000, v19
	v_fmac_f32_e32 v18, 0xbc800000, v130
	v_pk_mul_f32 v[140:141], v[38:39], v[38:39]
	v_pk_mul_f32 v[142:143], v[46:47], v[46:47]
	v_pk_mul_f32 v[144:145], v[34:35], v[34:35]
	v_pk_mul_f32 v[146:147], v[42:43], v[42:43]
	v_pk_mul_f32 v[148:149], v[40:41], v[40:41]
	v_pk_mul_f32 v[154:155], v[48:49], v[48:49]
	v_pk_mul_f32 v[156:157], v[36:37], v[36:37]
	v_pk_mul_f32 v[158:159], v[44:45], v[44:45]
	v_pk_fma_f32 v[156:157], v[20:21], v[20:21], v[156:157]
	v_pk_fma_f32 v[158:159], v[28:29], v[28:29], v[158:159]
	v_pk_fma_f32 v[154:155], v[32:33], v[32:33], v[154:155]
	v_pk_fma_f32 v[148:149], v[24:25], v[24:25], v[148:149]
	v_pk_fma_f32 v[146:147], v[26:27], v[26:27], v[146:147]
	v_pk_fma_f32 v[144:145], v[18:19], v[18:19], v[144:145]
	v_pk_fma_f32 v[142:143], v[30:31], v[30:31], v[142:143]
	v_pk_fma_f32 v[140:141], v[22:23], v[22:23], v[140:141]
	v_permlane32_swap_b32_e32 v132, v131
	v_pk_add_f32 v[140:141], v[140:141], v[142:143]
	v_pk_add_f32 v[142:143], v[144:145], v[146:147]
	v_pk_add_f32 v[144:145], v[148:149], v[154:155]
	v_pk_add_f32 v[146:147], v[156:157], v[158:159]
	v_pk_add_f32 v[140:141], v[142:143], v[140:141]
	v_pk_add_f32 v[144:145], v[146:147], v[144:145]
	v_pk_mul_f32 v[122:123], v[122:123], v[38:39]
	v_pk_mov_b32 v[142:143], v[140:141], v[144:145] op_sel:[1,0]
	v_mov_b32_e32 v141, v145
	v_pk_add_f32 v[140:141], v[142:143], v[140:141]
	v_pk_mul_f32 v[126:127], v[126:127], v[46:47]
	v_pk_add_f32 v[140:141], v[140:141], v[140:141] op_sel:[0,1] op_sel_hi:[1,0]
	v_pk_mul_f32 v[114:115], v[114:115], v[34:35]
	v_mov_b32_e32 v130, v140
	s_nop 1
	v_permlane32_swap_b32_e32 v140, v130
	v_mov_b32_e32 v141, v132
	v_pk_add_f32 v[130:131], v[140:141], v[130:131]
	v_pk_mul_f32 v[118:119], v[118:119], v[42:43]
	v_pk_fma_f32 v[130:131], v[130:131], s[0:1], v[152:153] op_sel_hi:[1,0,0]
	v_pk_mul_f32 v[124:125], v[124:125], v[40:41]
	v_mul_f32_e32 v132, 0x4b800000, v131
	v_cmp_gt_f32_e32 vcc, s1, v131
	v_pk_mul_f32 v[128:129], v[128:129], v[48:49]
	v_pk_mul_f32 v[116:117], v[116:117], v[36:37]
	v_pk_mul_f32 v[120:121], v[120:121], v[44:45]
	v_cndmask_b32_e32 v131, v131, v132, vcc
	v_mul_f32_e32 v132, 0x4b800000, v130
	v_cmp_gt_f32_e64 s[0:1], s1, v130
	v_pk_fma_f32 v[112:113], v[112:113], v[28:29], v[120:121]
	v_pk_fma_f32 v[104:105], v[104:105], v[20:21], v[116:117]
	v_pk_fma_f32 v[108:109], v[108:109], v[32:33], v[128:129]
	v_pk_fma_f32 v[100:101], v[100:101], v[24:25], v[124:125]
	v_pk_fma_f32 v[110:111], v[110:111], v[26:27], v[118:119]
	v_pk_fma_f32 v[102:103], v[102:103], v[18:19], v[114:115]
	v_pk_fma_f32 v[106:107], v[106:107], v[30:31], v[126:127]
	v_pk_fma_f32 v[98:99], v[98:99], v[22:23], v[122:123]
	v_rsq_f32_e32 v131, v131
	v_cndmask_b32_e64 v130, v130, v132, s[0:1]
	v_pk_add_f32 v[98:99], v[98:99], v[106:107]
	v_pk_add_f32 v[102:103], v[102:103], v[110:111]
	v_pk_add_f32 v[100:101], v[100:101], v[108:109]
	v_pk_add_f32 v[104:105], v[104:105], v[112:113]
	v_rsq_f32_e32 v132, v130
	v_pk_add_f32 v[100:101], v[104:105], v[100:101]
	v_pk_add_f32 v[98:99], v[102:103], v[98:99]
	v_mul_f32_e32 v130, 0x45800000, v131
	v_add_f32_e32 v98, v98, v99
	v_add_f32_e32 v99, v100, v101
	v_add_f32_e32 v98, v98, v99
	v_mov_b32_e32 v99, v98
	v_pk_mul_f32 v[90:91], v[90:91], v[38:39]
	v_pk_mul_f32 v[94:95], v[94:95], v[46:47]
	v_pk_mul_f32 v[82:83], v[82:83], v[34:35]
	v_pk_mul_f32 v[86:87], v[86:87], v[42:43]
	v_cndmask_b32_e32 v130, v131, v130, vcc
	v_mul_f32_e32 v131, 0x45800000, v132
	v_permlane32_swap_b32_e32 v98, v99
	v_pk_fma_f32 v[78:79], v[78:79], v[26:27], v[86:87]
	v_pk_fma_f32 v[70:71], v[70:71], v[18:19], v[82:83]
	v_pk_fma_f32 v[74:75], v[74:75], v[30:31], v[94:95]
	v_pk_fma_f32 v[66:67], v[66:67], v[22:23], v[90:91]
	v_cndmask_b32_e64 v131, v132, v131, s[0:1]
	v_add_f32_e32 v98, v98, v99
	v_pk_add_f32 v[66:67], v[66:67], v[74:75]
	v_pk_add_f32 v[70:71], v[70:71], v[78:79]
	v_mul_f32_e32 v139, v160, v130
	v_mul_f32_e32 v98, v98, v131
	v_pk_add_f32 v[66:67], v[70:71], v[66:67]
	v_cmp_gt_u32_e32 vcc, 32, v1
	v_add_f32_e32 v66, v66, v67
	v_pk_mul_f32 v[92:93], v[92:93], v[40:41]
	v_cndmask_b32_e32 v67, v98, v139, vcc
	v_add_f32_e32 v67, s12, v67
	v_pk_mul_f32 v[96:97], v[96:97], v[48:49]
	v_pk_mul_f32 v[84:85], v[84:85], v[36:37]
	v_pk_mul_f32 v[88:89], v[88:89], v[44:45]
	v_mul_f32_e32 v67, 0xbfb8aa3b, v67
	v_pk_fma_f32 v[80:81], v[80:81], v[28:29], v[88:89]
	v_pk_fma_f32 v[72:73], v[72:73], v[20:21], v[84:85]
	v_pk_fma_f32 v[76:77], v[76:77], v[32:33], v[96:97]
	v_pk_fma_f32 v[68:69], v[68:69], v[24:25], v[92:93]
	v_exp_f32_e32 v70, v67
	v_pk_add_f32 v[68:69], v[68:69], v[76:77]
	v_pk_add_f32 v[72:73], v[72:73], v[80:81]
	v_cmp_lt_i32_e64 s[0:1], 0, v151
	v_pk_add_f32 v[68:69], v[72:73], v[68:69]
	v_mov_b32_e32 v137, v136
	v_add_f32_e32 v67, v68, v69
	v_add_f32_e32 v67, v66, v67
	v_add_f32_e32 v66, 1.0, v70
	v_rcp_f32_e32 v66, v66
	v_mov_b32_e32 v69, 0xff800000
	v_mov_b32_e32 v138, v133
	v_mov_b32_e32 v68, v67
	v_cndmask_b32_e64 v70, v69, v66, s[0:1]
	v_mbcnt_lo_u32_b32 v66, -1, 0
	v_mbcnt_hi_u32_b32 v66, -1, v66
	v_permlane32_swap_b32_e32 v136, v137
	v_permlane32_swap_b32_e32 v133, v138
	v_permlane32_swap_b32_e32 v67, v68
	v_and_b32_e32 v86, 64, v66
	s_mov_b32 s14, 8
	s_mov_b32 s13, 0
	v_mov_b32_e32 v66, 0
	s_waitcnt lgkmcnt(0)
